# speedup vs baseline: 1.0751x; 1.0074x over previous
.LBB0_4:
	s_load_dwordx2 s[2:3], s[0:1], 0x0
	s_load_dwordx2 s[0:1], s[0:1], 0x10
	v_and_b32_e32 v3, 7, v2
	v_bfe_u32 v4, v2, 3, 8
	v_bfe_u32 v5, v2, 11, 4
	v_bfe_u32 v6, v2, 15, 2
	v_lshrrev_b32_e32 v7, 17, v2
	v_lshrrev_b32_e32 v8, 7, v4
	v_lshl_or_b32 v8, v6, 1, v8
	v_and_b32_e32 v9, 0x7f, v4
	v_lshrrev_b32_e32 v10, 1, v5
	v_and_b32_e32 v11, 1, v5
	v_lshlrev_b32_e32 v3, 3, v3
	v_lshl_or_b32 v11, v11, 6, v3
	v_lshl_or_b32 v8, v8, 1, v7
	v_lshl_or_b32 v10, v10, 1, v7
	v_lshl_or_b32 v8, v8, 4, v10
	v_lshl_or_b32 v8, v8, 7, v9
	v_lshl_or_b32 v8, v8, 7, v11
	v_lshlrev_b32_e32 v12, 2, v8
	v_lshlrev_b32_e32 v0, 4, v2
	s_waitcnt lgkmcnt(0)
	global_load_dwordx4 v[4:7], v12, s[2:3]
	global_load_dwordx4 v[8:11], v12, s[2:3] offset:16
	s_waitcnt vmcnt(1)
	v_cvt_pk_bf16_f32 v4, v4, v5
	v_cvt_pk_bf16_f32 v5, v6, v7
	s_waitcnt vmcnt(0)
	v_cvt_pk_bf16_f32 v6, v8, v9
	v_cvt_pk_bf16_f32 v7, v10, v11
	global_store_dwordx4 v0, v[4:7], s[0:1]
	s_endpgm

_Z11gemm_kernelPKfPKDF16bS0_Pf:
	s_and_b32 s3, s2, 7
	s_ashr_i32 s14, s2, 3
	s_lshl_b32 s12, s3, 6
	s_load_dwordx8 s[4:11], s[0:1], 0x0
	s_add_i32 s12, s12, s14
	s_bfe_u32 s18, s2, 0x10002
	s_lshl_b32 s2, s12, 6
	s_lshl_b32 s13, s18, 14
	s_and_b32 s2, s2, 0x3f00
	v_lshrrev_b32_e32 v52, 6, v0
	v_and_b32_e32 v50, 15, v0
	v_bfe_u32 v51, v0, 4, 2
	v_bfe_u32 v1, v0, 3, 3
	s_or_b32 s2, s2, s13
	v_lshl_or_b32 v102, v52, 2, v51
	v_lshl_or_b32 v104, v52, 3, v1
	v_lshlrev_b32_e32 v1, 4, v50
	s_lshl_b32 s15, s2, 9
	s_waitcnt lgkmcnt(0)
	v_and_b32_e32 v238, 3, v52
	v_lshlrev_b32_e32 v238, 6, v238
	v_lshl_or_b32 v238, v51, 2, v238
	v_lshlrev_b32_e32 v238, 2, v238
	s_and_b32 s24, s12, 3
	s_lshl_b32 s24, s24, 8
	s_lshl_b32 s25, s18, 10
	s_add_u32 s24, s24, s25
	s_lshl_b32 s24, s24, 2
	s_add_u32 s24, s8, s24
	s_addc_u32 s25, s9, 0
	global_load_dwordx4 v[240:243], v238, s[24:25]
	global_load_dwordx4 v[244:247], v238, s[24:25] offset:64
	global_load_dwordx4 v[248:251], v238, s[24:25] offset:128
	global_load_dwordx4 v[252:255], v238, s[24:25] offset:192
	s_mov_b64 s[0:1], s[6:7]
	s_and_b32 s5, s5, 0xffff
	s_mov_b32 s7, 0x20000
	s_brev_b32 s6, -2
	v_lshl_or_b32 v1, v102, 9, v1
	s_or_b32 s2, s15, 0x4000
	s_lshl_b32 s14, s14, 8
	v_lshlrev_b32_e32 v103, 3, v0
	buffer_load_dwordx4 v[54:57], v1, s[4:7], s15 offen sc0 nt
	buffer_load_dwordx4 v[58:61], v1, s[4:7], s2 offen sc0 nt
	s_or_b32 s2, s15, 0x8000
	s_or_b32 s3, s15, 0xc000
	s_lshl_b32 s19, s18, 10
	s_and_b32 s20, s14, 0x300
	v_and_b32_e32 v105, 56, v103
	buffer_load_dwordx4 v[62:65], v1, s[4:7], s2 offen sc0 nt
	buffer_load_dwordx4 v[66:69], v1, s[4:7], s3 offen sc0 nt
	s_or_b32 s2, s15, 0x10000
	s_or_b32 s3, s15, 0x14000
	s_or_b32 s14, s19, s20
	v_lshlrev_b32_e32 v106, 1, v105
	buffer_load_dwordx4 v[70:73], v1, s[4:7], s2 offen sc0 nt
	buffer_load_dwordx4 v[74:77], v1, s[4:7], s3 offen sc0 nt
	s_or_b32 s2, s15, 0x18000
	s_or_b32 s3, s15, 0x1c000
	s_lshl_b32 s14, s14, 11
	buffer_load_dwordx4 v[78:81], v1, s[4:7], s2 offen sc0 nt
	buffer_load_dwordx4 v[82:85], v1, s[4:7], s3 offen sc0 nt
	s_and_b32 s1, s1, 0xffff
	s_mov_b32 s2, s6
	s_mov_b32 s3, s7
	v_lshl_or_b32 v188, v104, 7, v106
	s_or_b32 s16, s14, 0x2000
	buffer_load_dwordx4 v[86:89], v188, s[0:3], s14 offen sc1
	buffer_load_dwordx4 v[90:93], v188, s[0:3], s16 offen sc1
	s_or_b32 s16, s14, 0x4000
	s_or_b32 s17, s14, 0x6000
	buffer_load_dwordx4 v[94:97], v188, s[0:3], s16 offen sc1
	buffer_load_dwordx4 v[98:101], v188, s[0:3], s17 offen sc1
	s_or_b32 s16, s15, 0x100
	s_or_b32 s17, s15, 0x4100
	buffer_load_dwordx4 v[10:13], v1, s[4:7], s16 offen sc0 nt
	buffer_load_dwordx4 v[18:21], v1, s[4:7], s17 offen sc0 nt
	s_or_b32 s16, s15, 0x8100
	s_or_b32 s17, s15, 0xc100
	buffer_load_dwordx4 v[22:25], v1, s[4:7], s16 offen sc0 nt
	buffer_load_dwordx4 v[30:33], v1, s[4:7], s17 offen sc0 nt
	s_or_b32 s16, s15, 0x10100
	s_or_b32 s17, s15, 0x14100
	buffer_load_dwordx4 v[34:37], v1, s[4:7], s16 offen sc0 nt
	buffer_load_dwordx4 v[38:41], v1, s[4:7], s17 offen sc0 nt
	s_or_b32 s16, s15, 0x18100
	s_or_b32 s15, s15, 0x1c100
	buffer_load_dwordx4 v[42:45], v1, s[4:7], s16 offen sc0 nt
	buffer_load_dwordx4 v[46:49], v1, s[4:7], s15 offen sc0 nt
	s_or_b32 s15, s14, 0x8000
	s_or_b32 s16, s14, 0xa000
	buffer_load_dwordx4 v[2:5], v188, s[0:3], s15 offen sc1
	buffer_load_dwordx4 v[6:9], v188, s[0:3], s16 offen sc1
	s_or_b32 s15, s14, 0xc000
	s_or_b32 s16, s14, 0xe000
	buffer_load_dwordx4 v[14:17], v188, s[0:3], s15 offen sc1
	buffer_load_dwordx4 v[26:29], v188, s[0:3], s16 offen sc1
	v_lshrrev_b32_e32 v107, 7, v0
	v_bfe_u32 v108, v0, 3, 1
	v_lshlrev_b32_e32 v102, 6, v102
	s_movk_i32 s2, 0x3c0
	v_and_or_b32 v102, v102, s2, v105
	v_lshrrev_b32_e32 v105, 2, v0
	v_and_or_b32 v107, v107, 2, v108
	v_and_b32_e32 v105, 32, v105
	v_lshlrev_b32_e32 v107, 10, v107
	v_bfe_u32 v103, v103, 5, 1
	v_lshlrev_b32_e32 v104, 6, v104
	v_and_b32_e32 v106, 48, v106
	v_bitop3_b32 v189, v102, v107, v105 bitop3:0xde
	v_and_or_b32 v103, v52, 6, v103
	v_and_or_b32 v104, v104, s2, v106
	v_lshrrev_b32_e32 v106, 1, v0
	v_lshlrev_b32_e32 v103, 10, v103
	v_and_b32_e32 v106, 32, v106
	v_bitop3_b32 v190, v104, v103, v106 bitop3:0xde
	v_lshrrev_b32_e32 v53, 8, v0
	s_movk_i32 s15, 0x4000
	s_mov_b32 s16, 0x8000
	s_mov_b32 s17, 0xc000
	s_waitcnt vmcnt(23)
	v_cvt_pk_bf16_f32 v57, v56, v57
	v_cvt_pk_bf16_f32 v56, v54, v55
	s_waitcnt vmcnt(22)
	v_cvt_pk_bf16_f32 v55, v60, v61
	v_cvt_pk_bf16_f32 v54, v58, v59
	ds_write2st64_b64 v189, v[56:57], v[54:55] offset1:8
	s_waitcnt vmcnt(21)
	v_cvt_pk_bf16_f32 v55, v64, v65
	v_cvt_pk_bf16_f32 v54, v62, v63
	s_waitcnt vmcnt(20)
	v_cvt_pk_bf16_f32 v57, v68, v69
	v_cvt_pk_bf16_f32 v56, v66, v67
	ds_write2st64_b64 v189, v[54:55], v[56:57] offset0:16 offset1:24
	s_waitcnt vmcnt(19)
	v_cvt_pk_bf16_f32 v55, v72, v73
	v_cvt_pk_bf16_f32 v54, v70, v71
	s_waitcnt vmcnt(18)
	v_cvt_pk_bf16_f32 v57, v76, v77
	v_cvt_pk_bf16_f32 v56, v74, v75
	ds_write2st64_b64 v189, v[54:55], v[56:57] offset0:32 offset1:40
	s_waitcnt vmcnt(17)
	v_cvt_pk_bf16_f32 v55, v80, v81
	v_cvt_pk_bf16_f32 v54, v78, v79
	s_waitcnt vmcnt(16)
	v_cvt_pk_bf16_f32 v57, v84, v85
	v_cvt_pk_bf16_f32 v56, v82, v83
	ds_write2st64_b64 v189, v[54:55], v[56:57] offset0:48 offset1:56
	s_waitcnt vmcnt(15)
	ds_write_b128 v190, v[86:89] offset:32768
	s_waitcnt vmcnt(14)
	ds_write_b128 v190, v[90:93] offset:40960
	s_waitcnt vmcnt(13)
	ds_write_b128 v190, v[94:97] offset:49152
	s_waitcnt vmcnt(12)
	ds_write_b128 v190, v[98:101] offset:57344
	s_waitcnt lgkmcnt(0)
	s_barrier
	v_cmp_eq_u32_e32 vcc, 1, v53
	s_and_saveexec_b64 s[2:3], vcc
	s_cbranch_execz .LBB1_2
	s_barrier

.LBB1_4:
	v_add_u32_e32 v182, s19, v191
	v_add_u32_e32 v238, s19, v192
	ds_read_b128 v[178:181], v182 offset:32768
	ds_read_b128 v[194:197], v182 offset:34816
	ds_read_b128 v[198:201], v182 offset:36864
	ds_read_b128 v[202:205], v182 offset:38912
	ds_read_b128 v[206:209], v238
	ds_read_b128 v[210:213], v238 offset:2048
	ds_read_b128 v[214:217], v238 offset:4096
	ds_read_b128 v[218:221], v238 offset:6144
	ds_read_b128 v[222:225], v238 offset:8192
	ds_read_b128 v[226:229], v238 offset:10240
	ds_read_b128 v[230:233], v238 offset:12288
	ds_read_b128 v[234:237], v238 offset:14336
	s_min_u32 s21, s20, 29
	s_xor_b32 s19, s19, 0x10000
	v_add_u32_e32 v239, s19, v189
	s_waitcnt vmcnt(11)
	v_cvt_pk_bf16_f32 v13, v12, v13
	v_cvt_pk_bf16_f32 v12, v10, v11
	s_waitcnt vmcnt(10)
	v_cvt_pk_bf16_f32 v11, v20, v21
	v_cvt_pk_bf16_f32 v10, v18, v19
	ds_write2st64_b64 v239, v[12:13], v[10:11] offset1:8
	s_waitcnt vmcnt(9)
	v_cvt_pk_bf16_f32 v11, v24, v25
	v_cvt_pk_bf16_f32 v10, v22, v23
	s_waitcnt vmcnt(8)
	v_cvt_pk_bf16_f32 v13, v32, v33
	v_cvt_pk_bf16_f32 v12, v30, v31
	ds_write2st64_b64 v239, v[10:11], v[12:13] offset0:16 offset1:24
	s_waitcnt vmcnt(7)
	v_cvt_pk_bf16_f32 v11, v36, v37
	v_cvt_pk_bf16_f32 v10, v34, v35
	s_waitcnt vmcnt(6)
	v_cvt_pk_bf16_f32 v13, v40, v41
	v_cvt_pk_bf16_f32 v12, v38, v39
	ds_write2st64_b64 v239, v[10:11], v[12:13] offset0:32 offset1:40
	s_waitcnt vmcnt(5)
	v_cvt_pk_bf16_f32 v11, v44, v45
	v_cvt_pk_bf16_f32 v10, v42, v43
	s_waitcnt vmcnt(4)
	v_cvt_pk_bf16_f32 v13, v48, v49
	v_cvt_pk_bf16_f32 v12, v46, v47
	ds_write2st64_b64 v239, v[10:11], v[12:13] offset0:48 offset1:56
	s_waitcnt lgkmcnt(0)
	s_add_i32 s21, s21, 2
	s_barrier
	s_waitcnt lgkmcnt(11)
	v_mfma_f32_16x16x32_bf16 v[174:177], v[178:181], v[206:209], v[174:177]
	s_lshl_b32 s22, s21, 1
	s_and_b32 s22, s22, 0x60
	s_add_i32 s22, s22, s12
	s_lshl_b32 s22, s22, 6
	v_mfma_f32_16x16x32_bf16 v[170:173], v[194:197], v[206:209], v[170:173]
	s_and_b32 s22, s22, 0x3f00
	s_or_b32 s22, s22, s13
	s_lshl_b32 s23, s21, 23
	s_lshl_b32 s22, s22, 9
	v_mfma_f32_16x16x32_bf16 v[158:161], v[198:201], v[206:209], v[158:161]
	s_and_b32 s23, s23, 0x7000000
	s_or_b32 s22, s22, s23
	s_lshl_b32 s23, s21, 8
	s_and_b32 s23, s23, 0x100
	s_or_b32 s22, s22, s23
	s_or_b32 s23, s22, 0x4000
	buffer_load_dwordx4 v[10:13], v1, s[4:7], s22 offen sc0 nt
	v_mfma_f32_16x16x32_bf16 v[142:145], v[202:205], v[206:209], v[142:145]
	s_waitcnt lgkmcnt(10)
	v_mfma_f32_16x16x32_bf16 v[166:169], v[178:181], v[210:213], v[166:169]
	v_mfma_f32_16x16x32_bf16 v[162:165], v[194:197], v[210:213], v[162:165]
	v_mfma_f32_16x16x32_bf16 v[146:149], v[198:201], v[210:213], v[146:149]
	buffer_load_dwordx4 v[18:21], v1, s[4:7], s23 offen sc0 nt
	s_or_b32 s23, s22, 0x8000
	v_mfma_f32_16x16x32_bf16 v[122:125], v[202:205], v[210:213], v[122:125]
	s_waitcnt lgkmcnt(9)
	v_mfma_f32_16x16x32_bf16 v[154:157], v[178:181], v[214:217], v[154:157]
	v_mfma_f32_16x16x32_bf16 v[150:153], v[194:197], v[214:217], v[150:153]
	v_mfma_f32_16x16x32_bf16 v[130:133], v[198:201], v[214:217], v[130:133]
	buffer_load_dwordx4 v[22:25], v1, s[4:7], s23 offen sc0 nt
	s_or_b32 s23, s22, 0xc000
	v_mfma_f32_16x16x32_bf16 v[106:109], v[202:205], v[214:217], v[106:109]
	s_waitcnt lgkmcnt(8)
	v_mfma_f32_16x16x32_bf16 v[138:141], v[178:181], v[218:221], v[138:141]
	v_mfma_f32_16x16x32_bf16 v[134:137], v[194:197], v[218:221], v[134:137]
	v_mfma_f32_16x16x32_bf16 v[114:117], v[198:201], v[218:221], v[114:117]
	buffer_load_dwordx4 v[30:33], v1, s[4:7], s23 offen sc0 nt
	s_or_b32 s23, s22, 0x10000
	v_mfma_f32_16x16x32_bf16 v[90:93], v[202:205], v[218:221], v[90:93]
	s_waitcnt lgkmcnt(7)
	v_mfma_f32_16x16x32_bf16 v[126:129], v[178:181], v[222:225], v[126:129]
	v_mfma_f32_16x16x32_bf16 v[118:121], v[194:197], v[222:225], v[118:121]
	v_mfma_f32_16x16x32_bf16 v[98:101], v[198:201], v[222:225], v[98:101]
	buffer_load_dwordx4 v[34:37], v1, s[4:7], s23 offen sc0 nt
	s_or_b32 s23, s22, 0x14000
	v_mfma_f32_16x16x32_bf16 v[74:77], v[202:205], v[222:225], v[74:77]
	s_waitcnt lgkmcnt(6)
	v_mfma_f32_16x16x32_bf16 v[110:113], v[178:181], v[226:229], v[110:113]
	v_mfma_f32_16x16x32_bf16 v[102:105], v[194:197], v[226:229], v[102:105]
	v_mfma_f32_16x16x32_bf16 v[82:85], v[198:201], v[226:229], v[82:85]
	buffer_load_dwordx4 v[38:41], v1, s[4:7], s23 offen sc0 nt
	s_or_b32 s23, s22, 0x18000
	s_or_b32 s22, s22, 0x1c000
	v_mfma_f32_16x16x32_bf16 v[62:65], v[202:205], v[226:229], v[62:65]
	s_waitcnt lgkmcnt(5)
	v_mfma_f32_16x16x32_bf16 v[94:97], v[178:181], v[230:233], v[94:97]
	v_mfma_f32_16x16x32_bf16 v[86:89], v[194:197], v[230:233], v[86:89]
	v_mfma_f32_16x16x32_bf16 v[70:73], v[198:201], v[230:233], v[70:73]
	buffer_load_dwordx4 v[42:45], v1, s[4:7], s23 offen sc0 nt
	v_mfma_f32_16x16x32_bf16 v[54:57], v[202:205], v[230:233], v[54:57]
	s_waitcnt lgkmcnt(4)
	v_mfma_f32_16x16x32_bf16 v[78:81], v[178:181], v[234:237], v[78:81]
	v_mfma_f32_16x16x32_bf16 v[66:69], v[194:197], v[234:237], v[66:69]
	v_mfma_f32_16x16x32_bf16 v[58:61], v[198:201], v[234:237], v[58:61]
	buffer_load_dwordx4 v[46:49], v1, s[4:7], s22 offen sc0 nt
	v_mfma_f32_16x16x32_bf16 v[50:53], v[202:205], v[234:237], v[50:53]
	s_waitcnt lgkmcnt(0)
	s_barrier
	ds_read_b128 v[178:181], v182 offset:33792
	ds_read_b128 v[194:197], v182 offset:35840
	ds_read_b128 v[198:201], v182 offset:37888
	ds_read_b128 v[202:205], v182 offset:39936
	ds_read_b128 v[206:209], v238 offset:1024
	ds_read_b128 v[210:213], v238 offset:3072
	ds_read_b128 v[214:217], v238 offset:5120
	ds_read_b128 v[218:221], v238 offset:7168
	ds_read_b128 v[222:225], v238 offset:9216
	ds_read_b128 v[226:229], v238 offset:11264
	ds_read_b128 v[230:233], v238 offset:13312
	ds_read_b128 v[234:237], v238 offset:15360
	v_add_u32_e32 v182, s19, v190
	s_waitcnt vmcnt(11)
	ds_write_b128 v182, v[2:5] offset:32768
	s_waitcnt vmcnt(10)
	ds_write_b128 v182, v[6:9] offset:40960
	s_waitcnt vmcnt(9)
	ds_write_b128 v182, v[14:17] offset:49152
	s_waitcnt vmcnt(8)
	ds_write_b128 v182, v[26:29] offset:57344
	s_waitcnt lgkmcnt(0)
	s_barrier
	s_waitcnt lgkmcnt(11)
	v_mfma_f32_16x16x32_bf16 v[174:177], v[178:181], v[206:209], v[174:177]
	s_lshl_b32 s21, s21, 15
	s_and_b32 s21, s21, 0x78000
	s_or_b32 s21, s21, s14
	s_or_b32 s22, s21, 0x2000
	v_mfma_f32_16x16x32_bf16 v[170:173], v[194:197], v[206:209], v[170:173]
	v_mfma_f32_16x16x32_bf16 v[158:161], v[198:201], v[206:209], v[158:161]
	v_mfma_f32_16x16x32_bf16 v[142:145], v[202:205], v[206:209], v[142:145]
	s_waitcnt lgkmcnt(10)
	v_mfma_f32_16x16x32_bf16 v[166:169], v[178:181], v[210:213], v[166:169]
	v_mfma_f32_16x16x32_bf16 v[162:165], v[194:197], v[210:213], v[162:165]
	buffer_load_dwordx4 v[2:5], v188, s[0:3], s21 offen sc1
	v_mfma_f32_16x16x32_bf16 v[146:149], v[198:201], v[210:213], v[146:149]
	v_mfma_f32_16x16x32_bf16 v[122:125], v[202:205], v[210:213], v[122:125]
	s_waitcnt lgkmcnt(9)
	v_mfma_f32_16x16x32_bf16 v[154:157], v[178:181], v[214:217], v[154:157]
	v_mfma_f32_16x16x32_bf16 v[150:153], v[194:197], v[214:217], v[150:153]
	v_mfma_f32_16x16x32_bf16 v[130:133], v[198:201], v[214:217], v[130:133]
	v_mfma_f32_16x16x32_bf16 v[106:109], v[202:205], v[214:217], v[106:109]
	s_waitcnt lgkmcnt(8)
	v_mfma_f32_16x16x32_bf16 v[138:141], v[178:181], v[218:221], v[138:141]
	v_mfma_f32_16x16x32_bf16 v[134:137], v[194:197], v[218:221], v[134:137]
	buffer_load_dwordx4 v[6:9], v188, s[0:3], s22 offen sc1
	s_or_b32 s22, s21, 0x4000
	s_or_b32 s21, s21, 0x6000
	v_mfma_f32_16x16x32_bf16 v[114:117], v[198:201], v[218:221], v[114:117]
	v_mfma_f32_16x16x32_bf16 v[90:93], v[202:205], v[218:221], v[90:93]
	s_waitcnt lgkmcnt(7)
	v_mfma_f32_16x16x32_bf16 v[126:129], v[178:181], v[222:225], v[126:129]
	v_mfma_f32_16x16x32_bf16 v[118:121], v[194:197], v[222:225], v[118:121]
	v_mfma_f32_16x16x32_bf16 v[98:101], v[198:201], v[222:225], v[98:101]
	v_mfma_f32_16x16x32_bf16 v[74:77], v[202:205], v[222:225], v[74:77]
	s_waitcnt lgkmcnt(6)
	v_mfma_f32_16x16x32_bf16 v[110:113], v[178:181], v[226:229], v[110:113]
	v_mfma_f32_16x16x32_bf16 v[102:105], v[194:197], v[226:229], v[102:105]
	buffer_load_dwordx4 v[14:17], v188, s[0:3], s22 offen sc1
	v_mfma_f32_16x16x32_bf16 v[82:85], v[198:201], v[226:229], v[82:85]
	v_mfma_f32_16x16x32_bf16 v[62:65], v[202:205], v[226:229], v[62:65]
	s_waitcnt lgkmcnt(5)
	v_mfma_f32_16x16x32_bf16 v[94:97], v[178:181], v[230:233], v[94:97]
	v_mfma_f32_16x16x32_bf16 v[86:89], v[194:197], v[230:233], v[86:89]
	v_mfma_f32_16x16x32_bf16 v[70:73], v[198:201], v[230:233], v[70:73]
	v_mfma_f32_16x16x32_bf16 v[54:57], v[202:205], v[230:233], v[54:57]
	s_waitcnt lgkmcnt(4)
	v_mfma_f32_16x16x32_bf16 v[78:81], v[178:181], v[234:237], v[78:81]
	v_mfma_f32_16x16x32_bf16 v[66:69], v[194:197], v[234:237], v[66:69]
	buffer_load_dwordx4 v[26:29], v188, s[0:3], s21 offen sc1
	v_mfma_f32_16x16x32_bf16 v[58:61], v[198:201], v[234:237], v[58:61]
	v_mfma_f32_16x16x32_bf16 v[50:53], v[202:205], v[234:237], v[50:53]
	s_and_b32 s21, s20, 15
	s_cmp_lg_u32 s21, 15
	s_cbranch_scc1 .LBB1_3
	s_and_b32 s21, s18, 32
	s_add_i32 s21, s21, s12
	s_lshl_b32 s21, s21, 6
	s_and_b32 s21, s21, 0x3f00
	v_add_lshl_u32 v182, v193, s21, 9
	v_lshl_add_u64 v[206:207], v[184:185], 0, v[182:183]
	v_add_co_u32_e32 v208, vcc, s8, v206
	s_nop 1
	v_addc_co_u32_e32 v209, vcc, 0, v207, vcc
	v_add_co_u32_e32 v210, vcc, s15, v206
	s_nop 1
	v_addc_co_u32_e32 v211, vcc, 0, v207, vcc
	v_add_co_u32_e32 v212, vcc, s9, v206
	s_nop 1
	v_addc_co_u32_e32 v213, vcc, 0, v207, vcc
	v_add_co_u32_e32 v214, vcc, s16, v206
	s_nop 1
	v_addc_co_u32_e32 v215, vcc, 0, v207, vcc
	v_add_co_u32_e32 v216, vcc, s10, v206
	s_nop 1
	v_addc_co_u32_e32 v217, vcc, 0, v207, vcc
	v_add_co_u32_e32 v218, vcc, s17, v206
	s_nop 1
	v_addc_co_u32_e32 v219, vcc, 0, v207, vcc
	v_add_co_u32_e32 v220, vcc, s11, v206
	s_nop 1
	v_addc_co_u32_e32 v221, vcc, 0, v207, vcc
	global_store_dwordx4 v[206:207], v[174:177], off
	global_store_dwordx4 v[206:207], v[170:173], off offset:64
	global_store_dwordx4 v[206:207], v[158:161], off offset:128
	global_store_dwordx4 v[206:207], v[142:145], off offset:192
	global_store_dwordx4 v[208:209], v[166:169], off
	global_store_dwordx4 v[208:209], v[162:165], off offset:64
	global_store_dwordx4 v[208:209], v[146:149], off offset:128
	global_store_dwordx4 v[208:209], v[122:125], off offset:192
	global_store_dwordx4 v[210:211], v[154:157], off
	global_store_dwordx4 v[210:211], v[150:153], off offset:64
	global_store_dwordx4 v[210:211], v[130:133], off offset:128
	global_store_dwordx4 v[210:211], v[106:109], off offset:192
	global_store_dwordx4 v[212:213], v[138:141], off
	global_store_dwordx4 v[212:213], v[134:137], off offset:64
	global_store_dwordx4 v[212:213], v[114:117], off offset:128
	global_store_dwordx4 v[212:213], v[90:93], off offset:192
	global_store_dwordx4 v[214:215], v[126:129], off
	global_store_dwordx4 v[214:215], v[118:121], off offset:64
	global_store_dwordx4 v[214:215], v[98:101], off offset:128
	global_store_dwordx4 v[214:215], v[74:77], off offset:192
	global_store_dwordx4 v[216:217], v[110:113], off
	global_store_dwordx4 v[216:217], v[102:105], off offset:64
	global_store_dwordx4 v[216:217], v[82:85], off offset:128
	global_store_dwordx4 v[216:217], v[62:65], off offset:192
	global_store_dwordx4 v[218:219], v[94:97], off
	global_store_dwordx4 v[218:219], v[86:89], off offset:64
	global_store_dwordx4 v[218:219], v[70:73], off offset:128
	global_store_dwordx4 v[218:219], v[54:57], off offset:192
	global_store_dwordx4 v[220:221], v[78:81], off
	global_store_dwordx4 v[220:221], v[66:69], off offset:64
	global_store_dwordx4 v[220:221], v[58:61], off offset:128
	global_store_dwordx4 v[220:221], v[50:53], off offset:192
.Lpd_tail:
	s_waitcnt lgkmcnt(0)
	s_barrier
	s_add_i32 s20, s20, 1
	s_add_i32 s18, s18, 2
	v_add_u32_e32 v182, s19, v191
	v_add_u32_e32 v238, s19, v192
	ds_read_b128 v[178:181], v182 offset:32768
	ds_read_b128 v[194:197], v182 offset:34816
	ds_read_b128 v[198:201], v182 offset:36864
	ds_read_b128 v[202:205], v182 offset:38912
	ds_read_b128 v[206:209], v238
	ds_read_b128 v[210:213], v238 offset:2048
	ds_read_b128 v[214:217], v238 offset:4096
	ds_read_b128 v[218:221], v238 offset:6144
	ds_read_b128 v[222:225], v238 offset:8192
	ds_read_b128 v[226:229], v238 offset:10240
	ds_read_b128 v[230:233], v238 offset:12288
	ds_read_b128 v[234:237], v238 offset:14336
	s_min_u32 s21, s20, 29
	s_xor_b32 s19, s19, 0x10000
	v_add_u32_e32 v239, s19, v189
	s_waitcnt vmcnt(43)
	v_cvt_pk_bf16_f32 v13, v12, v13
	v_cvt_pk_bf16_f32 v12, v10, v11
	s_waitcnt vmcnt(42)
	v_cvt_pk_bf16_f32 v11, v20, v21
	v_cvt_pk_bf16_f32 v10, v18, v19
	ds_write2st64_b64 v239, v[12:13], v[10:11] offset1:8
	s_waitcnt vmcnt(41)
	v_cvt_pk_bf16_f32 v11, v24, v25
	v_cvt_pk_bf16_f32 v10, v22, v23
	s_waitcnt vmcnt(40)
	v_cvt_pk_bf16_f32 v13, v32, v33
	v_cvt_pk_bf16_f32 v12, v30, v31
	ds_write2st64_b64 v239, v[10:11], v[12:13] offset0:16 offset1:24
	s_waitcnt vmcnt(39)
	v_cvt_pk_bf16_f32 v11, v36, v37
	v_cvt_pk_bf16_f32 v10, v34, v35
	s_waitcnt vmcnt(38)
	v_cvt_pk_bf16_f32 v13, v40, v41
	v_cvt_pk_bf16_f32 v12, v38, v39
	ds_write2st64_b64 v239, v[10:11], v[12:13] offset0:32 offset1:40
	s_waitcnt vmcnt(37)
	v_cvt_pk_bf16_f32 v11, v44, v45
	v_cvt_pk_bf16_f32 v10, v42, v43
	s_waitcnt vmcnt(36)
	v_cvt_pk_bf16_f32 v13, v48, v49
	v_cvt_pk_bf16_f32 v12, v46, v47
	ds_write2st64_b64 v239, v[10:11], v[12:13] offset0:48 offset1:56
	s_waitcnt lgkmcnt(0)
	s_add_i32 s21, s21, 2
	s_barrier
	s_waitcnt lgkmcnt(11)
	v_mfma_f32_16x16x32_bf16 v[174:177], v[178:181], v[206:209], v[240:243]
	s_lshl_b32 s22, s21, 1
	s_and_b32 s22, s22, 0x60
	s_add_i32 s22, s22, s12
	s_lshl_b32 s22, s22, 6
	v_mfma_f32_16x16x32_bf16 v[170:173], v[194:197], v[206:209], v[244:247]
	s_and_b32 s22, s22, 0x3f00
	s_or_b32 s22, s22, s13
	s_lshl_b32 s23, s21, 23
	s_lshl_b32 s22, s22, 9
	v_mfma_f32_16x16x32_bf16 v[158:161], v[198:201], v[206:209], v[248:251]
	s_and_b32 s23, s23, 0x7000000
	s_or_b32 s22, s22, s23
	s_lshl_b32 s23, s21, 8
	s_and_b32 s23, s23, 0x100
	s_or_b32 s22, s22, s23
	s_or_b32 s23, s22, 0x4000
	buffer_load_dwordx4 v[10:13], v1, s[4:7], s22 offen sc0 nt
	v_mfma_f32_16x16x32_bf16 v[142:145], v[202:205], v[206:209], v[252:255]
	s_waitcnt lgkmcnt(10)
	v_mfma_f32_16x16x32_bf16 v[166:169], v[178:181], v[210:213], v[240:243]
	v_mfma_f32_16x16x32_bf16 v[162:165], v[194:197], v[210:213], v[244:247]
	v_mfma_f32_16x16x32_bf16 v[146:149], v[198:201], v[210:213], v[248:251]
	buffer_load_dwordx4 v[18:21], v1, s[4:7], s23 offen sc0 nt
	s_or_b32 s23, s22, 0x8000
	v_mfma_f32_16x16x32_bf16 v[122:125], v[202:205], v[210:213], v[252:255]
	s_waitcnt lgkmcnt(9)
	v_mfma_f32_16x16x32_bf16 v[154:157], v[178:181], v[214:217], v[240:243]
	v_mfma_f32_16x16x32_bf16 v[150:153], v[194:197], v[214:217], v[244:247]
	v_mfma_f32_16x16x32_bf16 v[130:133], v[198:201], v[214:217], v[248:251]
	buffer_load_dwordx4 v[22:25], v1, s[4:7], s23 offen sc0 nt
	s_or_b32 s23, s22, 0xc000
	v_mfma_f32_16x16x32_bf16 v[106:109], v[202:205], v[214:217], v[252:255]
	s_waitcnt lgkmcnt(8)
	v_mfma_f32_16x16x32_bf16 v[138:141], v[178:181], v[218:221], v[240:243]
	v_mfma_f32_16x16x32_bf16 v[134:137], v[194:197], v[218:221], v[244:247]
	v_mfma_f32_16x16x32_bf16 v[114:117], v[198:201], v[218:221], v[248:251]
	buffer_load_dwordx4 v[30:33], v1, s[4:7], s23 offen sc0 nt
	s_or_b32 s23, s22, 0x10000
	v_mfma_f32_16x16x32_bf16 v[90:93], v[202:205], v[218:221], v[252:255]
	s_waitcnt lgkmcnt(7)
	v_mfma_f32_16x16x32_bf16 v[126:129], v[178:181], v[222:225], v[240:243]
	v_mfma_f32_16x16x32_bf16 v[118:121], v[194:197], v[222:225], v[244:247]
	v_mfma_f32_16x16x32_bf16 v[98:101], v[198:201], v[222:225], v[248:251]
	buffer_load_dwordx4 v[34:37], v1, s[4:7], s23 offen sc0 nt
	s_or_b32 s23, s22, 0x14000
	v_mfma_f32_16x16x32_bf16 v[74:77], v[202:205], v[222:225], v[252:255]
	s_waitcnt lgkmcnt(6)
	v_mfma_f32_16x16x32_bf16 v[110:113], v[178:181], v[226:229], v[240:243]
	v_mfma_f32_16x16x32_bf16 v[102:105], v[194:197], v[226:229], v[244:247]
	v_mfma_f32_16x16x32_bf16 v[82:85], v[198:201], v[226:229], v[248:251]
	buffer_load_dwordx4 v[38:41], v1, s[4:7], s23 offen sc0 nt
	s_or_b32 s23, s22, 0x18000
	s_or_b32 s22, s22, 0x1c000
	v_mfma_f32_16x16x32_bf16 v[62:65], v[202:205], v[226:229], v[252:255]
	s_waitcnt lgkmcnt(5)
	v_mfma_f32_16x16x32_bf16 v[94:97], v[178:181], v[230:233], v[240:243]
	v_mfma_f32_16x16x32_bf16 v[86:89], v[194:197], v[230:233], v[244:247]
	v_mfma_f32_16x16x32_bf16 v[70:73], v[198:201], v[230:233], v[248:251]
	buffer_load_dwordx4 v[42:45], v1, s[4:7], s23 offen sc0 nt
	v_mfma_f32_16x16x32_bf16 v[54:57], v[202:205], v[230:233], v[252:255]
	s_waitcnt lgkmcnt(4)
	v_mfma_f32_16x16x32_bf16 v[78:81], v[178:181], v[234:237], v[240:243]
	v_mfma_f32_16x16x32_bf16 v[66:69], v[194:197], v[234:237], v[244:247]
	v_mfma_f32_16x16x32_bf16 v[58:61], v[198:201], v[234:237], v[248:251]
	buffer_load_dwordx4 v[46:49], v1, s[4:7], s22 offen sc0 nt
	v_mfma_f32_16x16x32_bf16 v[50:53], v[202:205], v[234:237], v[252:255]
	s_waitcnt lgkmcnt(0)
	s_barrier
	ds_read_b128 v[178:181], v182 offset:33792
	ds_read_b128 v[194:197], v182 offset:35840
	ds_read_b128 v[198:201], v182 offset:37888
	ds_read_b128 v[202:205], v182 offset:39936
	ds_read_b128 v[206:209], v238 offset:1024
	ds_read_b128 v[210:213], v238 offset:3072
	ds_read_b128 v[214:217], v238 offset:5120
	ds_read_b128 v[218:221], v238 offset:7168
	ds_read_b128 v[222:225], v238 offset:9216
	ds_read_b128 v[226:229], v238 offset:11264
	ds_read_b128 v[230:233], v238 offset:13312
	ds_read_b128 v[234:237], v238 offset:15360
	v_add_u32_e32 v182, s19, v190
	s_waitcnt vmcnt(43)
	ds_write_b128 v182, v[2:5] offset:32768
	s_waitcnt vmcnt(42)
	ds_write_b128 v182, v[6:9] offset:40960
	s_waitcnt vmcnt(41)
	ds_write_b128 v182, v[14:17] offset:49152
	s_waitcnt vmcnt(40)
	ds_write_b128 v182, v[26:29] offset:57344
	s_waitcnt lgkmcnt(0)
	s_barrier
	s_waitcnt lgkmcnt(11)
	v_mfma_f32_16x16x32_bf16 v[174:177], v[178:181], v[206:209], v[174:177]
	s_lshl_b32 s21, s21, 15
	s_and_b32 s21, s21, 0x78000
	s_or_b32 s21, s21, s14
	s_or_b32 s22, s21, 0x2000
	v_mfma_f32_16x16x32_bf16 v[170:173], v[194:197], v[206:209], v[170:173]
	v_mfma_f32_16x16x32_bf16 v[158:161], v[198:201], v[206:209], v[158:161]
	v_mfma_f32_16x16x32_bf16 v[142:145], v[202:205], v[206:209], v[142:145]
	s_waitcnt lgkmcnt(10)
	v_mfma_f32_16x16x32_bf16 v[166:169], v[178:181], v[210:213], v[166:169]
	v_mfma_f32_16x16x32_bf16 v[162:165], v[194:197], v[210:213], v[162:165]
	buffer_load_dwordx4 v[2:5], v188, s[0:3], s21 offen sc1
	v_mfma_f32_16x16x32_bf16 v[146:149], v[198:201], v[210:213], v[146:149]
	v_mfma_f32_16x16x32_bf16 v[122:125], v[202:205], v[210:213], v[122:125]
	s_waitcnt lgkmcnt(9)
	v_mfma_f32_16x16x32_bf16 v[154:157], v[178:181], v[214:217], v[154:157]
	v_mfma_f32_16x16x32_bf16 v[150:153], v[194:197], v[214:217], v[150:153]
	v_mfma_f32_16x16x32_bf16 v[130:133], v[198:201], v[214:217], v[130:133]
	v_mfma_f32_16x16x32_bf16 v[106:109], v[202:205], v[214:217], v[106:109]
	s_waitcnt lgkmcnt(8)
	v_mfma_f32_16x16x32_bf16 v[138:141], v[178:181], v[218:221], v[138:141]
	v_mfma_f32_16x16x32_bf16 v[134:137], v[194:197], v[218:221], v[134:137]
	buffer_load_dwordx4 v[6:9], v188, s[0:3], s22 offen sc1
	s_or_b32 s22, s21, 0x4000
	s_or_b32 s21, s21, 0x6000
	v_mfma_f32_16x16x32_bf16 v[114:117], v[198:201], v[218:221], v[114:117]
	v_mfma_f32_16x16x32_bf16 v[90:93], v[202:205], v[218:221], v[90:93]
	s_waitcnt lgkmcnt(7)
	v_mfma_f32_16x16x32_bf16 v[126:129], v[178:181], v[222:225], v[126:129]
	v_mfma_f32_16x16x32_bf16 v[118:121], v[194:197], v[222:225], v[118:121]
	v_mfma_f32_16x16x32_bf16 v[98:101], v[198:201], v[222:225], v[98:101]
	v_mfma_f32_16x16x32_bf16 v[74:77], v[202:205], v[222:225], v[74:77]
	s_waitcnt lgkmcnt(6)
	v_mfma_f32_16x16x32_bf16 v[110:113], v[178:181], v[226:229], v[110:113]
	v_mfma_f32_16x16x32_bf16 v[102:105], v[194:197], v[226:229], v[102:105]
	buffer_load_dwordx4 v[14:17], v188, s[0:3], s22 offen sc1
	v_mfma_f32_16x16x32_bf16 v[82:85], v[198:201], v[226:229], v[82:85]
	v_mfma_f32_16x16x32_bf16 v[62:65], v[202:205], v[226:229], v[62:65]
	s_waitcnt lgkmcnt(5)
	v_mfma_f32_16x16x32_bf16 v[94:97], v[178:181], v[230:233], v[94:97]
	v_mfma_f32_16x16x32_bf16 v[86:89], v[194:197], v[230:233], v[86:89]
	v_mfma_f32_16x16x32_bf16 v[70:73], v[198:201], v[230:233], v[70:73]
	v_mfma_f32_16x16x32_bf16 v[54:57], v[202:205], v[230:233], v[54:57]
	s_waitcnt lgkmcnt(4)
	v_mfma_f32_16x16x32_bf16 v[78:81], v[178:181], v[234:237], v[78:81]
	v_mfma_f32_16x16x32_bf16 v[66:69], v[194:197], v[234:237], v[66:69]
	buffer_load_dwordx4 v[26:29], v188, s[0:3], s21 offen sc1
	v_mfma_f32_16x16x32_bf16 v[58:61], v[198:201], v[234:237], v[58:61]
	v_mfma_f32_16x16x32_bf16 v[50:53], v[202:205], v[234:237], v[50:53]
	s_branch .LBB1_3
.Lt30:
	v_add_u32_e32 v182, s19, v191
	v_add_u32_e32 v238, s19, v192
	ds_read_b128 v[178:181], v182 offset:32768
	ds_read_b128 v[194:197], v182 offset:34816
	ds_read_b128 v[198:201], v182 offset:36864
	ds_read_b128 v[202:205], v182 offset:38912
	ds_read_b128 v[206:209], v238
	ds_read_b128 v[210:213], v238 offset:2048
	ds_read_b128 v[214:217], v238 offset:4096
	ds_read_b128 v[218:221], v238 offset:6144
	ds_read_b128 v[222:225], v238 offset:8192
	ds_read_b128 v[226:229], v238 offset:10240
	ds_read_b128 v[230:233], v238 offset:12288
	ds_read_b128 v[234:237], v238 offset:14336
	s_min_u32 s21, s20, 29
	s_xor_b32 s19, s19, 0x10000
	v_add_u32_e32 v239, s19, v189
	s_waitcnt vmcnt(11)
	v_cvt_pk_bf16_f32 v13, v12, v13
	v_cvt_pk_bf16_f32 v12, v10, v11
	s_waitcnt vmcnt(10)
	v_cvt_pk_bf16_f32 v11, v20, v21
	v_cvt_pk_bf16_f32 v10, v18, v19
	ds_write2st64_b64 v239, v[12:13], v[10:11] offset1:8
	s_waitcnt vmcnt(9)
	v_cvt_pk_bf16_f32 v11, v24, v25
	v_cvt_pk_bf16_f32 v10, v22, v23
	s_waitcnt vmcnt(8)
	v_cvt_pk_bf16_f32 v13, v32, v33
	v_cvt_pk_bf16_f32 v12, v30, v31
	ds_write2st64_b64 v239, v[10:11], v[12:13] offset0:16 offset1:24
	s_waitcnt vmcnt(7)
	v_cvt_pk_bf16_f32 v11, v36, v37
	v_cvt_pk_bf16_f32 v10, v34, v35
	s_waitcnt vmcnt(6)
	v_cvt_pk_bf16_f32 v13, v40, v41
	v_cvt_pk_bf16_f32 v12, v38, v39
	ds_write2st64_b64 v239, v[10:11], v[12:13] offset0:32 offset1:40
	s_waitcnt vmcnt(5)
	v_cvt_pk_bf16_f32 v11, v44, v45
	v_cvt_pk_bf16_f32 v10, v42, v43
	s_waitcnt vmcnt(4)
	v_cvt_pk_bf16_f32 v13, v48, v49
	v_cvt_pk_bf16_f32 v12, v46, v47
	ds_write2st64_b64 v239, v[10:11], v[12:13] offset0:48 offset1:56
	s_waitcnt lgkmcnt(0)
	s_add_i32 s21, s21, 2
	s_barrier
	s_waitcnt lgkmcnt(11)
	v_mfma_f32_16x16x32_bf16 v[174:177], v[178:181], v[206:209], v[174:177]
	s_lshl_b32 s22, s21, 1
	s_and_b32 s22, s22, 0x60
	s_add_i32 s22, s22, s12
	s_lshl_b32 s22, s22, 6
	v_mfma_f32_16x16x32_bf16 v[170:173], v[194:197], v[206:209], v[170:173]
	s_and_b32 s22, s22, 0x3f00
	s_or_b32 s22, s22, s13
	s_lshl_b32 s23, s21, 23
	s_lshl_b32 s22, s22, 9
	v_mfma_f32_16x16x32_bf16 v[158:161], v[198:201], v[206:209], v[158:161]
	s_and_b32 s23, s23, 0x7000000
	s_or_b32 s22, s22, s23
	s_lshl_b32 s23, s21, 8
	s_and_b32 s23, s23, 0x100
	s_or_b32 s22, s22, s23
	s_or_b32 s23, s22, 0x4000
	v_mfma_f32_16x16x32_bf16 v[142:145], v[202:205], v[206:209], v[142:145]
	s_waitcnt lgkmcnt(10)
	v_mfma_f32_16x16x32_bf16 v[166:169], v[178:181], v[210:213], v[166:169]
	v_mfma_f32_16x16x32_bf16 v[162:165], v[194:197], v[210:213], v[162:165]
	v_mfma_f32_16x16x32_bf16 v[146:149], v[198:201], v[210:213], v[146:149]
	s_or_b32 s23, s22, 0x8000
	v_mfma_f32_16x16x32_bf16 v[122:125], v[202:205], v[210:213], v[122:125]
	s_waitcnt lgkmcnt(9)
	v_mfma_f32_16x16x32_bf16 v[154:157], v[178:181], v[214:217], v[154:157]
	v_mfma_f32_16x16x32_bf16 v[150:153], v[194:197], v[214:217], v[150:153]
	v_mfma_f32_16x16x32_bf16 v[130:133], v[198:201], v[214:217], v[130:133]
	s_or_b32 s23, s22, 0xc000
	v_mfma_f32_16x16x32_bf16 v[106:109], v[202:205], v[214:217], v[106:109]
	s_waitcnt lgkmcnt(8)
	v_mfma_f32_16x16x32_bf16 v[138:141], v[178:181], v[218:221], v[138:141]
	v_mfma_f32_16x16x32_bf16 v[134:137], v[194:197], v[218:221], v[134:137]
	v_mfma_f32_16x16x32_bf16 v[114:117], v[198:201], v[218:221], v[114:117]
	s_or_b32 s23, s22, 0x10000
	v_mfma_f32_16x16x32_bf16 v[90:93], v[202:205], v[218:221], v[90:93]
	s_waitcnt lgkmcnt(7)
	v_mfma_f32_16x16x32_bf16 v[126:129], v[178:181], v[222:225], v[126:129]
	v_mfma_f32_16x16x32_bf16 v[118:121], v[194:197], v[222:225], v[118:121]
	v_mfma_f32_16x16x32_bf16 v[98:101], v[198:201], v[222:225], v[98:101]
	s_or_b32 s23, s22, 0x14000
	v_mfma_f32_16x16x32_bf16 v[74:77], v[202:205], v[222:225], v[74:77]
	s_waitcnt lgkmcnt(6)
	v_mfma_f32_16x16x32_bf16 v[110:113], v[178:181], v[226:229], v[110:113]
	v_mfma_f32_16x16x32_bf16 v[102:105], v[194:197], v[226:229], v[102:105]
	v_mfma_f32_16x16x32_bf16 v[82:85], v[198:201], v[226:229], v[82:85]
	s_or_b32 s23, s22, 0x18000
	s_or_b32 s22, s22, 0x1c000
	v_mfma_f32_16x16x32_bf16 v[62:65], v[202:205], v[226:229], v[62:65]
	s_waitcnt lgkmcnt(5)
	v_mfma_f32_16x16x32_bf16 v[94:97], v[178:181], v[230:233], v[94:97]
	v_mfma_f32_16x16x32_bf16 v[86:89], v[194:197], v[230:233], v[86:89]
	v_mfma_f32_16x16x32_bf16 v[70:73], v[198:201], v[230:233], v[70:73]
	v_mfma_f32_16x16x32_bf16 v[54:57], v[202:205], v[230:233], v[54:57]
	s_waitcnt lgkmcnt(4)
	v_mfma_f32_16x16x32_bf16 v[78:81], v[178:181], v[234:237], v[78:81]
	v_mfma_f32_16x16x32_bf16 v[66:69], v[194:197], v[234:237], v[66:69]
	v_mfma_f32_16x16x32_bf16 v[58:61], v[198:201], v[234:237], v[58:61]
	v_mfma_f32_16x16x32_bf16 v[50:53], v[202:205], v[234:237], v[50:53]
	s_waitcnt lgkmcnt(0)
	s_barrier
	ds_read_b128 v[178:181], v182 offset:33792
	ds_read_b128 v[194:197], v182 offset:35840
	ds_read_b128 v[198:201], v182 offset:37888
	ds_read_b128 v[202:205], v182 offset:39936
	ds_read_b128 v[206:209], v238 offset:1024
	ds_read_b128 v[210:213], v238 offset:3072
	ds_read_b128 v[214:217], v238 offset:5120
	ds_read_b128 v[218:221], v238 offset:7168
	ds_read_b128 v[222:225], v238 offset:9216
	ds_read_b128 v[226:229], v238 offset:11264
	ds_read_b128 v[230:233], v238 offset:13312
	ds_read_b128 v[234:237], v238 offset:15360
	v_add_u32_e32 v182, s19, v190
	s_waitcnt vmcnt(3)
	ds_write_b128 v182, v[2:5] offset:32768
	s_waitcnt vmcnt(2)
	ds_write_b128 v182, v[6:9] offset:40960
	s_waitcnt vmcnt(1)
	ds_write_b128 v182, v[14:17] offset:49152
	s_waitcnt vmcnt(0)
	ds_write_b128 v182, v[26:29] offset:57344
	s_waitcnt lgkmcnt(0)
	s_barrier
	s_waitcnt lgkmcnt(11)
	v_mfma_f32_16x16x32_bf16 v[174:177], v[178:181], v[206:209], v[174:177]
	s_lshl_b32 s21, s21, 15
	s_and_b32 s21, s21, 0x78000
	s_or_b32 s21, s21, s14
	s_or_b32 s22, s21, 0x2000
	v_mfma_f32_16x16x32_bf16 v[170:173], v[194:197], v[206:209], v[170:173]
	v_mfma_f32_16x16x32_bf16 v[158:161], v[198:201], v[206:209], v[158:161]
	v_mfma_f32_16x16x32_bf16 v[142:145], v[202:205], v[206:209], v[142:145]
	s_waitcnt lgkmcnt(10)
	v_mfma_f32_16x16x32_bf16 v[166:169], v[178:181], v[210:213], v[166:169]
	v_mfma_f32_16x16x32_bf16 v[162:165], v[194:197], v[210:213], v[162:165]
	v_mfma_f32_16x16x32_bf16 v[146:149], v[198:201], v[210:213], v[146:149]
	v_mfma_f32_16x16x32_bf16 v[122:125], v[202:205], v[210:213], v[122:125]
	s_waitcnt lgkmcnt(9)
	v_mfma_f32_16x16x32_bf16 v[154:157], v[178:181], v[214:217], v[154:157]
	v_mfma_f32_16x16x32_bf16 v[150:153], v[194:197], v[214:217], v[150:153]
	v_mfma_f32_16x16x32_bf16 v[130:133], v[198:201], v[214:217], v[130:133]
	v_mfma_f32_16x16x32_bf16 v[106:109], v[202:205], v[214:217], v[106:109]
	s_waitcnt lgkmcnt(8)
	v_mfma_f32_16x16x32_bf16 v[138:141], v[178:181], v[218:221], v[138:141]
	v_mfma_f32_16x16x32_bf16 v[134:137], v[194:197], v[218:221], v[134:137]
	s_or_b32 s22, s21, 0x4000
	s_or_b32 s21, s21, 0x6000
	v_mfma_f32_16x16x32_bf16 v[114:117], v[198:201], v[218:221], v[114:117]
	v_mfma_f32_16x16x32_bf16 v[90:93], v[202:205], v[218:221], v[90:93]
	s_waitcnt lgkmcnt(7)
	v_mfma_f32_16x16x32_bf16 v[126:129], v[178:181], v[222:225], v[126:129]
	v_mfma_f32_16x16x32_bf16 v[118:121], v[194:197], v[222:225], v[118:121]
	v_mfma_f32_16x16x32_bf16 v[98:101], v[198:201], v[222:225], v[98:101]
	v_mfma_f32_16x16x32_bf16 v[74:77], v[202:205], v[222:225], v[74:77]
	s_waitcnt lgkmcnt(6)
	v_mfma_f32_16x16x32_bf16 v[110:113], v[178:181], v[226:229], v[110:113]
	v_mfma_f32_16x16x32_bf16 v[102:105], v[194:197], v[226:229], v[102:105]
	v_mfma_f32_16x16x32_bf16 v[82:85], v[198:201], v[226:229], v[82:85]
	v_mfma_f32_16x16x32_bf16 v[62:65], v[202:205], v[226:229], v[62:65]
	s_waitcnt lgkmcnt(5)
	v_mfma_f32_16x16x32_bf16 v[94:97], v[178:181], v[230:233], v[94:97]
	v_mfma_f32_16x16x32_bf16 v[86:89], v[194:197], v[230:233], v[86:89]
	v_mfma_f32_16x16x32_bf16 v[70:73], v[198:201], v[230:233], v[70:73]
	v_mfma_f32_16x16x32_bf16 v[54:57], v[202:205], v[230:233], v[54:57]
	s_waitcnt lgkmcnt(4)
	v_mfma_f32_16x16x32_bf16 v[78:81], v[178:181], v[234:237], v[78:81]
	v_mfma_f32_16x16x32_bf16 v[66:69], v[194:197], v[234:237], v[66:69]
	v_mfma_f32_16x16x32_bf16 v[58:61], v[198:201], v[234:237], v[58:61]
	v_mfma_f32_16x16x32_bf16 v[50:53], v[202:205], v[234:237], v[50:53]
	s_waitcnt lgkmcnt(0)
	s_barrier
	s_add_i32 s20, s20, 1
	s_add_i32 s18, s18, 2
	v_add_u32_e32 v182, s19, v191
	v_add_u32_e32 v238, s19, v192
	ds_read_b128 v[178:181], v182 offset:32768
	ds_read_b128 v[194:197], v182 offset:34816
	ds_read_b128 v[198:201], v182 offset:36864
	ds_read_b128 v[202:205], v182 offset:38912
	ds_read_b128 v[206:209], v238
	ds_read_b128 v[210:213], v238 offset:2048
	ds_read_b128 v[214:217], v238 offset:4096
	ds_read_b128 v[218:221], v238 offset:6144
	ds_read_b128 v[222:225], v238 offset:8192
	ds_read_b128 v[226:229], v238 offset:10240
	ds_read_b128 v[230:233], v238 offset:12288
	ds_read_b128 v[234:237], v238 offset:14336
	s_min_u32 s21, s20, 29
	s_xor_b32 s19, s19, 0x10000
	v_add_u32_e32 v239, s19, v189
	s_waitcnt lgkmcnt(0)
	s_add_i32 s21, s21, 2
	s_barrier
	s_waitcnt lgkmcnt(11)
	v_mfma_f32_16x16x32_bf16 v[174:177], v[178:181], v[206:209], v[174:177]
	s_lshl_b32 s22, s21, 1
	s_and_b32 s22, s22, 0x60
	s_add_i32 s22, s22, s12
	s_lshl_b32 s22, s22, 6
	v_mfma_f32_16x16x32_bf16 v[170:173], v[194:197], v[206:209], v[170:173]
	s_and_b32 s22, s22, 0x3f00
	s_or_b32 s22, s22, s13
	s_lshl_b32 s23, s21, 23
	s_lshl_b32 s22, s22, 9
	v_mfma_f32_16x16x32_bf16 v[158:161], v[198:201], v[206:209], v[158:161]
	s_and_b32 s23, s23, 0x7000000
	s_or_b32 s22, s22, s23
	s_lshl_b32 s23, s21, 8
	s_and_b32 s23, s23, 0x100
	s_or_b32 s22, s22, s23
	s_or_b32 s23, s22, 0x4000
	v_mfma_f32_16x16x32_bf16 v[142:145], v[202:205], v[206:209], v[142:145]
	s_waitcnt lgkmcnt(10)
	v_mfma_f32_16x16x32_bf16 v[166:169], v[178:181], v[210:213], v[166:169]
	v_mfma_f32_16x16x32_bf16 v[162:165], v[194:197], v[210:213], v[162:165]
	v_mfma_f32_16x16x32_bf16 v[146:149], v[198:201], v[210:213], v[146:149]
	s_or_b32 s23, s22, 0x8000
	v_mfma_f32_16x16x32_bf16 v[122:125], v[202:205], v[210:213], v[122:125]
	s_waitcnt lgkmcnt(9)
	v_mfma_f32_16x16x32_bf16 v[154:157], v[178:181], v[214:217], v[154:157]
	v_mfma_f32_16x16x32_bf16 v[150:153], v[194:197], v[214:217], v[150:153]
	v_mfma_f32_16x16x32_bf16 v[130:133], v[198:201], v[214:217], v[130:133]
	s_or_b32 s23, s22, 0xc000
	v_mfma_f32_16x16x32_bf16 v[106:109], v[202:205], v[214:217], v[106:109]
	s_waitcnt lgkmcnt(8)
	v_mfma_f32_16x16x32_bf16 v[138:141], v[178:181], v[218:221], v[138:141]
	v_mfma_f32_16x16x32_bf16 v[134:137], v[194:197], v[218:221], v[134:137]
	v_mfma_f32_16x16x32_bf16 v[114:117], v[198:201], v[218:221], v[114:117]
	s_or_b32 s23, s22, 0x10000
	v_mfma_f32_16x16x32_bf16 v[90:93], v[202:205], v[218:221], v[90:93]
	s_waitcnt lgkmcnt(7)
	v_mfma_f32_16x16x32_bf16 v[126:129], v[178:181], v[222:225], v[126:129]
	v_mfma_f32_16x16x32_bf16 v[118:121], v[194:197], v[222:225], v[118:121]
	v_mfma_f32_16x16x32_bf16 v[98:101], v[198:201], v[222:225], v[98:101]
	s_or_b32 s23, s22, 0x14000
	v_mfma_f32_16x16x32_bf16 v[74:77], v[202:205], v[222:225], v[74:77]
	s_waitcnt lgkmcnt(6)
	v_mfma_f32_16x16x32_bf16 v[110:113], v[178:181], v[226:229], v[110:113]
	v_mfma_f32_16x16x32_bf16 v[102:105], v[194:197], v[226:229], v[102:105]
	v_mfma_f32_16x16x32_bf16 v[82:85], v[198:201], v[226:229], v[82:85]
	s_or_b32 s23, s22, 0x18000
	s_or_b32 s22, s22, 0x1c000
	v_mfma_f32_16x16x32_bf16 v[62:65], v[202:205], v[226:229], v[62:65]
	s_waitcnt lgkmcnt(5)
	v_mfma_f32_16x16x32_bf16 v[94:97], v[178:181], v[230:233], v[94:97]
	v_mfma_f32_16x16x32_bf16 v[86:89], v[194:197], v[230:233], v[86:89]
	v_mfma_f32_16x16x32_bf16 v[70:73], v[198:201], v[230:233], v[70:73]
	v_mfma_f32_16x16x32_bf16 v[54:57], v[202:205], v[230:233], v[54:57]
	s_waitcnt lgkmcnt(4)
	v_mfma_f32_16x16x32_bf16 v[78:81], v[178:181], v[234:237], v[78:81]
	v_mfma_f32_16x16x32_bf16 v[66:69], v[194:197], v[234:237], v[66:69]
	v_mfma_f32_16x16x32_bf16 v[58:61], v[198:201], v[234:237], v[58:61]
	v_mfma_f32_16x16x32_bf16 v[50:53], v[202:205], v[234:237], v[50:53]
	s_waitcnt lgkmcnt(0)
	s_barrier
	ds_read_b128 v[178:181], v182 offset:33792
	ds_read_b128 v[194:197], v182 offset:35840
	ds_read_b128 v[198:201], v182 offset:37888
	ds_read_b128 v[202:205], v182 offset:39936
	ds_read_b128 v[206:209], v238 offset:1024
	ds_read_b128 v[210:213], v238 offset:3072
	ds_read_b128 v[214:217], v238 offset:5120
	ds_read_b128 v[218:221], v238 offset:7168
	ds_read_b128 v[222:225], v238 offset:9216
	ds_read_b128 v[226:229], v238 offset:11264
	ds_read_b128 v[230:233], v238 offset:13312
	ds_read_b128 v[234:237], v238 offset:15360
	s_waitcnt lgkmcnt(0)
	s_barrier
	s_waitcnt lgkmcnt(11)
	v_mfma_f32_16x16x32_bf16 v[174:177], v[178:181], v[206:209], v[174:177]
	s_lshl_b32 s21, s21, 15
	s_and_b32 s21, s21, 0x78000
	s_or_b32 s21, s21, s14
	s_or_b32 s22, s21, 0x2000
	v_mfma_f32_16x16x32_bf16 v[170:173], v[194:197], v[206:209], v[170:173]
	v_mfma_f32_16x16x32_bf16 v[158:161], v[198:201], v[206:209], v[158:161]
	v_mfma_f32_16x16x32_bf16 v[142:145], v[202:205], v[206:209], v[142:145]
	s_waitcnt lgkmcnt(10)
	v_mfma_f32_16x16x32_bf16 v[166:169], v[178:181], v[210:213], v[166:169]
	v_mfma_f32_16x16x32_bf16 v[162:165], v[194:197], v[210:213], v[162:165]
	v_mfma_f32_16x16x32_bf16 v[146:149], v[198:201], v[210:213], v[146:149]
	v_mfma_f32_16x16x32_bf16 v[122:125], v[202:205], v[210:213], v[122:125]
	s_waitcnt lgkmcnt(9)
	v_mfma_f32_16x16x32_bf16 v[154:157], v[178:181], v[214:217], v[154:157]
	v_mfma_f32_16x16x32_bf16 v[150:153], v[194:197], v[214:217], v[150:153]
	v_mfma_f32_16x16x32_bf16 v[130:133], v[198:201], v[214:217], v[130:133]
	v_mfma_f32_16x16x32_bf16 v[106:109], v[202:205], v[214:217], v[106:109]
	s_waitcnt lgkmcnt(8)
	v_mfma_f32_16x16x32_bf16 v[138:141], v[178:181], v[218:221], v[138:141]
	v_mfma_f32_16x16x32_bf16 v[134:137], v[194:197], v[218:221], v[134:137]
	s_or_b32 s22, s21, 0x4000
	s_or_b32 s21, s21, 0x6000
	v_mfma_f32_16x16x32_bf16 v[114:117], v[198:201], v[218:221], v[114:117]
	v_mfma_f32_16x16x32_bf16 v[90:93], v[202:205], v[218:221], v[90:93]
	s_waitcnt lgkmcnt(7)
	v_mfma_f32_16x16x32_bf16 v[126:129], v[178:181], v[222:225], v[126:129]
	v_mfma_f32_16x16x32_bf16 v[118:121], v[194:197], v[222:225], v[118:121]
	v_mfma_f32_16x16x32_bf16 v[98:101], v[198:201], v[222:225], v[98:101]
	v_mfma_f32_16x16x32_bf16 v[74:77], v[202:205], v[222:225], v[74:77]
	s_waitcnt lgkmcnt(6)
	v_mfma_f32_16x16x32_bf16 v[110:113], v[178:181], v[226:229], v[110:113]
	v_mfma_f32_16x16x32_bf16 v[102:105], v[194:197], v[226:229], v[102:105]
	v_mfma_f32_16x16x32_bf16 v[82:85], v[198:201], v[226:229], v[82:85]
	v_mfma_f32_16x16x32_bf16 v[62:65], v[202:205], v[226:229], v[62:65]
	s_waitcnt lgkmcnt(5)
	v_mfma_f32_16x16x32_bf16 v[94:97], v[178:181], v[230:233], v[94:97]
	v_mfma_f32_16x16x32_bf16 v[86:89], v[194:197], v[230:233], v[86:89]
	v_mfma_f32_16x16x32_bf16 v[70:73], v[198:201], v[230:233], v[70:73]
	v_mfma_f32_16x16x32_bf16 v[54:57], v[202:205], v[230:233], v[54:57]
	s_waitcnt lgkmcnt(4)
	v_mfma_f32_16x16x32_bf16 v[78:81], v[178:181], v[234:237], v[78:81]
	v_mfma_f32_16x16x32_bf16 v[66:69], v[194:197], v[234:237], v[66:69]
	v_mfma_f32_16x16x32_bf16 v[58:61], v[198:201], v[234:237], v[58:61]
	v_mfma_f32_16x16x32_bf16 v[50:53], v[202:205], v[234:237], v[50:53]
	s_and_b32 s21, s18, 32
	s_add_i32 s21, s21, s12
	s_lshl_b32 s21, s21, 6
	s_and_b32 s21, s21, 0x3f00
	v_add_lshl_u32 v182, v193, s21, 9
	v_lshl_add_u64 v[206:207], v[184:185], 0, v[182:183]
	v_add_co_u32_e32 v208, vcc, s8, v206
	s_nop 1
	v_addc_co_u32_e32 v209, vcc, 0, v207, vcc
	v_add_co_u32_e32 v210, vcc, s15, v206
	s_nop 1
	v_addc_co_u32_e32 v211, vcc, 0, v207, vcc
	v_add_co_u32_e32 v212, vcc, s9, v206
	s_nop 1
	v_addc_co_u32_e32 v213, vcc, 0, v207, vcc
	v_add_co_u32_e32 v214, vcc, s16, v206
	s_nop 1
	v_addc_co_u32_e32 v215, vcc, 0, v207, vcc
	v_add_co_u32_e32 v216, vcc, s10, v206
	s_nop 1
	v_addc_co_u32_e32 v217, vcc, 0, v207, vcc
	v_add_co_u32_e32 v218, vcc, s17, v206
	s_nop 1
	v_addc_co_u32_e32 v219, vcc, 0, v207, vcc
	v_add_co_u32_e32 v220, vcc, s11, v206
	s_nop 1
	v_addc_co_u32_e32 v221, vcc, 0, v207, vcc
	global_store_dwordx4 v[206:207], v[174:177], off
	global_store_dwordx4 v[206:207], v[170:173], off offset:64
	global_store_dwordx4 v[206:207], v[158:161], off offset:128
	global_store_dwordx4 v[206:207], v[142:145], off offset:192
	global_store_dwordx4 v[208:209], v[166:169], off
	global_store_dwordx4 v[208:209], v[162:165], off offset:64
	global_store_dwordx4 v[208:209], v[146:149], off offset:128
	global_store_dwordx4 v[208:209], v[122:125], off offset:192
	global_store_dwordx4 v[210:211], v[154:157], off
	global_store_dwordx4 v[210:211], v[150:153], off offset:64
	global_store_dwordx4 v[210:211], v[130:133], off offset:128
	global_store_dwordx4 v[210:211], v[106:109], off offset:192
	global_store_dwordx4 v[212:213], v[138:141], off
	global_store_dwordx4 v[212:213], v[134:137], off offset:64
	global_store_dwordx4 v[212:213], v[114:117], off offset:128
	global_store_dwordx4 v[212:213], v[90:93], off offset:192
	global_store_dwordx4 v[214:215], v[126:129], off
	global_store_dwordx4 v[214:215], v[118:121], off offset:64
	global_store_dwordx4 v[214:215], v[98:101], off offset:128
	global_store_dwordx4 v[214:215], v[74:77], off offset:192
	global_store_dwordx4 v[216:217], v[110:113], off
	global_store_dwordx4 v[216:217], v[102:105], off offset:64
	global_store_dwordx4 v[216:217], v[82:85], off offset:128
	global_store_dwordx4 v[216:217], v[62:65], off offset:192
	global_store_dwordx4 v[218:219], v[94:97], off
	global_store_dwordx4 v[218:219], v[86:89], off offset:64
	global_store_dwordx4 v[218:219], v[70:73], off offset:128
	global_store_dwordx4 v[218:219], v[54:57], off offset:192
	global_store_dwordx4 v[220:221], v[78:81], off
	global_store_dwordx4 v[220:221], v[66:69], off offset:64
	global_store_dwordx4 v[220:221], v[58:61], off offset:128
	global_store_dwordx4 v[220:221], v[50:53], off offset:192
	s_waitcnt lgkmcnt(0)
	s_barrier
	s_branch .LBB1_6
.Lfirst:
	v_add_u32_e32 v182, s19, v191
	v_add_u32_e32 v238, s19, v192
	ds_read_b128 v[178:181], v182 offset:32768
	ds_read_b128 v[194:197], v182 offset:34816
	ds_read_b128 v[198:201], v182 offset:36864
	ds_read_b128 v[202:205], v182 offset:38912
	ds_read_b128 v[206:209], v238
	ds_read_b128 v[210:213], v238 offset:2048
	ds_read_b128 v[214:217], v238 offset:4096
	ds_read_b128 v[218:221], v238 offset:6144
	ds_read_b128 v[222:225], v238 offset:8192
	ds_read_b128 v[226:229], v238 offset:10240
	ds_read_b128 v[230:233], v238 offset:12288
	ds_read_b128 v[234:237], v238 offset:14336
	s_min_u32 s21, s20, 29
	s_xor_b32 s19, s19, 0x10000
	v_add_u32_e32 v239, s19, v189
	s_waitcnt vmcnt(11)
	v_cvt_pk_bf16_f32 v13, v12, v13
	v_cvt_pk_bf16_f32 v12, v10, v11
	s_waitcnt vmcnt(10)
	v_cvt_pk_bf16_f32 v11, v20, v21
	v_cvt_pk_bf16_f32 v10, v18, v19
	ds_write2st64_b64 v239, v[12:13], v[10:11] offset1:8
	s_waitcnt vmcnt(9)
	v_cvt_pk_bf16_f32 v11, v24, v25
	v_cvt_pk_bf16_f32 v10, v22, v23
	s_waitcnt vmcnt(8)
	v_cvt_pk_bf16_f32 v13, v32, v33
	v_cvt_pk_bf16_f32 v12, v30, v31
	ds_write2st64_b64 v239, v[10:11], v[12:13] offset0:16 offset1:24
	s_waitcnt vmcnt(7)
	v_cvt_pk_bf16_f32 v11, v36, v37
	v_cvt_pk_bf16_f32 v10, v34, v35
	s_waitcnt vmcnt(6)
	v_cvt_pk_bf16_f32 v13, v40, v41
	v_cvt_pk_bf16_f32 v12, v38, v39
	ds_write2st64_b64 v239, v[10:11], v[12:13] offset0:32 offset1:40
	s_waitcnt vmcnt(5)
	v_cvt_pk_bf16_f32 v11, v44, v45
	v_cvt_pk_bf16_f32 v10, v42, v43
	s_waitcnt vmcnt(4)
	v_cvt_pk_bf16_f32 v13, v48, v49
	v_cvt_pk_bf16_f32 v12, v46, v47
	ds_write2st64_b64 v239, v[10:11], v[12:13] offset0:48 offset1:56
	s_waitcnt lgkmcnt(0)
	s_add_i32 s21, s21, 2
	s_barrier
	s_waitcnt lgkmcnt(11)
	v_mfma_f32_16x16x32_bf16 v[174:177], v[178:181], v[206:209], v[240:243]
	s_lshl_b32 s22, s21, 1
	s_and_b32 s22, s22, 0x60
	s_add_i32 s22, s22, s12
	s_lshl_b32 s22, s22, 6
	v_mfma_f32_16x16x32_bf16 v[170:173], v[194:197], v[206:209], v[244:247]
	s_and_b32 s22, s22, 0x3f00
	s_or_b32 s22, s22, s13
	s_lshl_b32 s23, s21, 23
	s_lshl_b32 s22, s22, 9
	v_mfma_f32_16x16x32_bf16 v[158:161], v[198:201], v[206:209], v[248:251]
	s_and_b32 s23, s23, 0x7000000
	s_or_b32 s22, s22, s23
	s_lshl_b32 s23, s21, 8
	s_and_b32 s23, s23, 0x100
	s_or_b32 s22, s22, s23
	s_or_b32 s23, s22, 0x4000
	buffer_load_dwordx4 v[10:13], v1, s[4:7], s22 offen sc0 nt
	v_mfma_f32_16x16x32_bf16 v[142:145], v[202:205], v[206:209], v[252:255]
	s_waitcnt lgkmcnt(10)
	v_mfma_f32_16x16x32_bf16 v[166:169], v[178:181], v[210:213], v[240:243]
	v_mfma_f32_16x16x32_bf16 v[162:165], v[194:197], v[210:213], v[244:247]
	v_mfma_f32_16x16x32_bf16 v[146:149], v[198:201], v[210:213], v[248:251]
	buffer_load_dwordx4 v[18:21], v1, s[4:7], s23 offen sc0 nt
	s_or_b32 s23, s22, 0x8000
	v_mfma_f32_16x16x32_bf16 v[122:125], v[202:205], v[210:213], v[252:255]
	s_waitcnt lgkmcnt(9)
	v_mfma_f32_16x16x32_bf16 v[154:157], v[178:181], v[214:217], v[240:243]
	v_mfma_f32_16x16x32_bf16 v[150:153], v[194:197], v[214:217], v[244:247]
	v_mfma_f32_16x16x32_bf16 v[130:133], v[198:201], v[214:217], v[248:251]
	buffer_load_dwordx4 v[22:25], v1, s[4:7], s23 offen sc0 nt
	s_or_b32 s23, s22, 0xc000
	v_mfma_f32_16x16x32_bf16 v[106:109], v[202:205], v[214:217], v[252:255]
	s_waitcnt lgkmcnt(8)
	v_mfma_f32_16x16x32_bf16 v[138:141], v[178:181], v[218:221], v[240:243]
	v_mfma_f32_16x16x32_bf16 v[134:137], v[194:197], v[218:221], v[244:247]
	v_mfma_f32_16x16x32_bf16 v[114:117], v[198:201], v[218:221], v[248:251]
	buffer_load_dwordx4 v[30:33], v1, s[4:7], s23 offen sc0 nt
	s_or_b32 s23, s22, 0x10000
	v_mfma_f32_16x16x32_bf16 v[90:93], v[202:205], v[218:221], v[252:255]
	s_waitcnt lgkmcnt(7)
	v_mfma_f32_16x16x32_bf16 v[126:129], v[178:181], v[222:225], v[240:243]
	v_mfma_f32_16x16x32_bf16 v[118:121], v[194:197], v[222:225], v[244:247]
	v_mfma_f32_16x16x32_bf16 v[98:101], v[198:201], v[222:225], v[248:251]
	buffer_load_dwordx4 v[34:37], v1, s[4:7], s23 offen sc0 nt
	s_or_b32 s23, s22, 0x14000
	v_mfma_f32_16x16x32_bf16 v[74:77], v[202:205], v[222:225], v[252:255]
	s_waitcnt lgkmcnt(6)
	v_mfma_f32_16x16x32_bf16 v[110:113], v[178:181], v[226:229], v[240:243]
	v_mfma_f32_16x16x32_bf16 v[102:105], v[194:197], v[226:229], v[244:247]
	v_mfma_f32_16x16x32_bf16 v[82:85], v[198:201], v[226:229], v[248:251]
	buffer_load_dwordx4 v[38:41], v1, s[4:7], s23 offen sc0 nt
	s_or_b32 s23, s22, 0x18000
	s_or_b32 s22, s22, 0x1c000
	v_mfma_f32_16x16x32_bf16 v[62:65], v[202:205], v[226:229], v[252:255]
	s_waitcnt lgkmcnt(5)
	v_mfma_f32_16x16x32_bf16 v[94:97], v[178:181], v[230:233], v[240:243]
	v_mfma_f32_16x16x32_bf16 v[86:89], v[194:197], v[230:233], v[244:247]
	v_mfma_f32_16x16x32_bf16 v[70:73], v[198:201], v[230:233], v[248:251]
	buffer_load_dwordx4 v[42:45], v1, s[4:7], s23 offen sc0 nt
	v_mfma_f32_16x16x32_bf16 v[54:57], v[202:205], v[230:233], v[252:255]
	s_waitcnt lgkmcnt(4)
	v_mfma_f32_16x16x32_bf16 v[78:81], v[178:181], v[234:237], v[240:243]
	v_mfma_f32_16x16x32_bf16 v[66:69], v[194:197], v[234:237], v[244:247]
	v_mfma_f32_16x16x32_bf16 v[58:61], v[198:201], v[234:237], v[248:251]
	buffer_load_dwordx4 v[46:49], v1, s[4:7], s22 offen sc0 nt
	v_mfma_f32_16x16x32_bf16 v[50:53], v[202:205], v[234:237], v[252:255]
	s_waitcnt lgkmcnt(0)
	s_barrier
	ds_read_b128 v[178:181], v182 offset:33792
	ds_read_b128 v[194:197], v182 offset:35840
	ds_read_b128 v[198:201], v182 offset:37888
	ds_read_b128 v[202:205], v182 offset:39936
	ds_read_b128 v[206:209], v238 offset:1024
	ds_read_b128 v[210:213], v238 offset:3072
	ds_read_b128 v[214:217], v238 offset:5120
	ds_read_b128 v[218:221], v238 offset:7168
	ds_read_b128 v[222:225], v238 offset:9216
	ds_read_b128 v[226:229], v238 offset:11264
	ds_read_b128 v[230:233], v238 offset:13312
	ds_read_b128 v[234:237], v238 offset:15360
	v_add_u32_e32 v182, s19, v190
	s_waitcnt vmcnt(11)
	ds_write_b128 v182, v[2:5] offset:32768
	s_waitcnt vmcnt(10)
	ds_write_b128 v182, v[6:9] offset:40960
	s_waitcnt vmcnt(9)
	ds_write_b128 v182, v[14:17] offset:49152
	s_waitcnt vmcnt(8)
	ds_write_b128 v182, v[26:29] offset:57344
	s_waitcnt lgkmcnt(0)
	s_barrier
	s_waitcnt lgkmcnt(11)
	v_mfma_f32_16x16x32_bf16 v[174:177], v[178:181], v[206:209], v[174:177]
	s_lshl_b32 s21, s21, 15
	s_and_b32 s21, s21, 0x78000
	s_or_b32 s21, s21, s14
	s_or_b32 s22, s21, 0x2000
	v_mfma_f32_16x16x32_bf16 v[170:173], v[194:197], v[206:209], v[170:173]
	v_mfma_f32_16x16x32_bf16 v[158:161], v[198:201], v[206:209], v[158:161]
	v_mfma_f32_16x16x32_bf16 v[142:145], v[202:205], v[206:209], v[142:145]
	s_waitcnt lgkmcnt(10)
	v_mfma_f32_16x16x32_bf16 v[166:169], v[178:181], v[210:213], v[166:169]
	v_mfma_f32_16x16x32_bf16 v[162:165], v[194:197], v[210:213], v[162:165]
	buffer_load_dwordx4 v[2:5], v188, s[0:3], s21 offen sc1
	v_mfma_f32_16x16x32_bf16 v[146:149], v[198:201], v[210:213], v[146:149]
	v_mfma_f32_16x16x32_bf16 v[122:125], v[202:205], v[210:213], v[122:125]
	s_waitcnt lgkmcnt(9)
	v_mfma_f32_16x16x32_bf16 v[154:157], v[178:181], v[214:217], v[154:157]
	v_mfma_f32_16x16x32_bf16 v[150:153], v[194:197], v[214:217], v[150:153]
	v_mfma_f32_16x16x32_bf16 v[130:133], v[198:201], v[214:217], v[130:133]
	v_mfma_f32_16x16x32_bf16 v[106:109], v[202:205], v[214:217], v[106:109]
	s_waitcnt lgkmcnt(8)
	v_mfma_f32_16x16x32_bf16 v[138:141], v[178:181], v[218:221], v[138:141]
	v_mfma_f32_16x16x32_bf16 v[134:137], v[194:197], v[218:221], v[134:137]
	buffer_load_dwordx4 v[6:9], v188, s[0:3], s22 offen sc1
	s_or_b32 s22, s21, 0x4000
	s_or_b32 s21, s21, 0x6000
	v_mfma_f32_16x16x32_bf16 v[114:117], v[198:201], v[218:221], v[114:117]
	v_mfma_f32_16x16x32_bf16 v[90:93], v[202:205], v[218:221], v[90:93]
	s_waitcnt lgkmcnt(7)
	v_mfma_f32_16x16x32_bf16 v[126:129], v[178:181], v[222:225], v[126:129]
	v_mfma_f32_16x16x32_bf16 v[118:121], v[194:197], v[222:225], v[118:121]
	v_mfma_f32_16x16x32_bf16 v[98:101], v[198:201], v[222:225], v[98:101]
	v_mfma_f32_16x16x32_bf16 v[74:77], v[202:205], v[222:225], v[74:77]
	s_waitcnt lgkmcnt(6)
	v_mfma_f32_16x16x32_bf16 v[110:113], v[178:181], v[226:229], v[110:113]
	v_mfma_f32_16x16x32_bf16 v[102:105], v[194:197], v[226:229], v[102:105]
	buffer_load_dwordx4 v[14:17], v188, s[0:3], s22 offen sc1
	v_mfma_f32_16x16x32_bf16 v[82:85], v[198:201], v[226:229], v[82:85]
	v_mfma_f32_16x16x32_bf16 v[62:65], v[202:205], v[226:229], v[62:65]
	s_waitcnt lgkmcnt(5)
	v_mfma_f32_16x16x32_bf16 v[94:97], v[178:181], v[230:233], v[94:97]
	v_mfma_f32_16x16x32_bf16 v[86:89], v[194:197], v[230:233], v[86:89]
	v_mfma_f32_16x16x32_bf16 v[70:73], v[198:201], v[230:233], v[70:73]
	v_mfma_f32_16x16x32_bf16 v[54:57], v[202:205], v[230:233], v[54:57]
	s_waitcnt lgkmcnt(4)
	v_mfma_f32_16x16x32_bf16 v[78:81], v[178:181], v[234:237], v[78:81]
	v_mfma_f32_16x16x32_bf16 v[66:69], v[194:197], v[234:237], v[66:69]
	buffer_load_dwordx4 v[26:29], v188, s[0:3], s21 offen sc1
	v_mfma_f32_16x16x32_bf16 v[58:61], v[198:201], v[234:237], v[58:61]
	v_mfma_f32_16x16x32_bf16 v[50:53], v[202:205], v[234:237], v[50:53]
	s_branch .LBB1_3
